# speedup vs baseline: 1.0374x; 1.0374x over previous
.LBB2_70:
	s_and_b64 vcc, exec, s[4:5]
	s_cbranch_vccz .LBB2_72
	s_load_dwordx4 s[4:7], s[0:1], 0x290
	s_waitcnt vmcnt(0)
	v_lshl_or_b32 v1, s2, 8, v0
	v_add_u32_e32 v10, 0xfffd2400, v1
	v_ashrrev_i32_e32 v11, 31, v10
	v_lshlrev_b64 v[2:3], 5, v[10:11]
	s_waitcnt lgkmcnt(0)
	v_lshl_add_u64 v[12:13], s[4:5], 0, v[2:3]
	global_load_dwordx4 v[2:5], v[12:13], off nt
	global_load_dwordx4 v[6:9], v[12:13], off offset:16 nt
	v_bfe_u32 v1, v0, 3, 2
	v_ashrrev_i32_e32 v10, 5, v10
	v_mov_b32_e32 v13, 0
	v_mul_u32_u24_e32 v12, 0xc350, v1
	v_ashrrev_i32_e32 v11, 31, v10
	v_lshl_add_u64 v[10:11], v[10:11], 0, v[12:13]
	v_lshlrev_b32_e32 v14, 4, v0
	v_lshlrev_b64 v[10:11], 7, v[10:11]
	v_and_b32_e32 v12, 0x70, v14
	v_lshl_add_u64 v[10:11], s[6:7], 0, v[10:11]
	s_waitcnt vmcnt(1)
	v_cvt_f16_f32_e32 v1, v2
	v_cvt_pk_f16_f32 v2, v3, v4
	s_waitcnt vmcnt(0)
	v_cvt_pk_f16_f32 v4, v5, v6
	v_cvt_f16_f32_e32 v6, v9
	v_cvt_pk_f16_f32 v5, v7, v8
	v_alignbit_b32 v3, v4, v2, 16
	v_alignbit_b32 v4, v5, v4, 16
	v_pack_b32_f16 v2, v1, v2
	v_alignbit_b32 v5, v6, v5, 16
	v_lshl_add_u64 v[6:7], v[10:11], 0, v[12:13]
	global_store_dwordx4 v[6:7], v[2:5], off

.LBB3_106:
	s_load_dwordx4 s[4:7], s[0:1], 0x20
	v_lshl_or_b32 v1, s2, 8, v0
	v_add_u32_e32 v10, 0xfffdb400, v1
	v_ashrrev_i32_e32 v11, 31, v10
	v_lshlrev_b64 v[2:3], 5, v[10:11]
	s_waitcnt lgkmcnt(0)
	v_lshl_add_u64 v[12:13], s[4:5], 0, v[2:3]
	global_load_dwordx4 v[2:5], v[12:13], off nt
	global_load_dwordx4 v[6:9], v[12:13], off offset:16 nt
	v_and_b32_e32 v1, 8, v0
	v_mov_b32_e32 v11, 0xc350
	v_lshlrev_b32_e32 v14, 4, v0
	v_cmp_eq_u32_e32 vcc, 0, v1
	v_ashrrev_i32_e32 v0, 4, v10
	v_mov_b32_e32 v13, 0
	v_cndmask_b32_e64 v12, v11, 0, vcc
	v_ashrrev_i32_e32 v1, 31, v0
	v_lshl_add_u64 v[0:1], v[12:13], 0, v[0:1]
	v_lshlrev_b64 v[0:1], 7, v[0:1]
	v_lshl_add_u64 v[10:11], s[6:7], 0, v[0:1]
	v_and_b32_e32 v12, 0x70, v14
	s_waitcnt vmcnt(1)
	v_cvt_f16_f32_e32 v0, v2
	s_waitcnt vmcnt(0)
	v_cvt_pk_f16_f32 v2, v5, v6
	v_cvt_f16_f32_e32 v5, v9
	v_cvt_pk_f16_f32 v3, v3, v4
	v_cvt_pk_f16_f32 v4, v7, v8
	v_alignbit_b32 v1, v2, v3, 16
	v_alignbit_b32 v2, v4, v2, 16
	v_pack_b32_f16 v0, v0, v3
	v_alignbit_b32 v3, v5, v4, 16
	v_lshl_add_u64 v[4:5], v[10:11], 0, v[12:13]
	global_store_dwordx4 v[4:5], v[0:3], off
	s_endpgm

.LBB4_72:
	v_sub_u32_e32 v0, v37, v36
	v_max_i32_e32 v0, 1, v0
	v_cvt_f32_u32_e32 v0, v0
	s_and_b64 s[0:1], s[20:21], exec
	s_waitcnt lgkmcnt(0)
	s_cselect_b32 s2, s10, s14
	s_cselect_b32 s3, s11, s15
	v_div_scale_f32 v1, s[0:1], v0, v0, 1.0
	v_rcp_f32_e32 v2, v1
	s_and_b64 s[0:1], s[18:19], exec
	s_cselect_b32 s3, s3, s7
	s_cselect_b32 s2, s2, s6
	v_fma_f32 v3, -v1, v2, 1.0
	v_fmac_f32_e32 v2, v3, v2
	v_div_scale_f32 v3, vcc, 1.0, v0, 1.0
	v_mul_f32_e32 v4, v3, v2
	v_fma_f32 v5, -v1, v4, v3
	v_fmac_f32_e32 v4, v5, v2
	v_fma_f32 v1, -v1, v4, v3
	v_div_fmas_f32 v1, v1, v2, v4
	v_div_fixup_f32 v4, v1, v0, 1.0
	s_lshl_b64 s[0:1], s[16:17], 1
	v_pk_mul_f32 v[0:1], v[4:5], v[38:39] op_sel_hi:[0,1]
	v_pk_mul_f32 v[2:3], v[4:5], v[42:43] op_sel_hi:[0,1]
	s_add_u32 s0, s2, s0
	v_cvt_pk_f16_f32 v0, v0, v1
	v_cvt_pk_f16_f32 v1, v2, v3
	v_pk_mul_f32 v[2:3], v[4:5], v[40:41] op_sel_hi:[0,1]
	v_pk_mul_f32 v[4:5], v[4:5], v[34:35] op_sel_hi:[0,1]
	s_addc_u32 s1, s3, s1
	v_cvt_pk_f16_f32 v2, v2, v3
	v_cvt_pk_f16_f32 v3, v4, v5
	s_and_b32 s1, s1, 0xffff
	s_mov_b32 s3, 0x20000
	s_mov_b32 s2, 0x61a800
	v_lshl_or_b32 v4, v32, 7, v33
	buffer_store_dwordx4 v[0:3], v4, s[0:3], 0 offen sc1
	s_endpgm

.LBB5_5:
	s_load_dwordx2 s[62:63], s[0:1], 0x20
	s_load_dwordx2 s[64:65], s[0:1], 0x50
	v_mov_b32_e32 v33, 0
	s_andn2_b64 vcc, exec, s[6:7]
	v_mov_b32_e32 v32, v33
	v_mov_b32_e32 v31, v33
	v_mov_b32_e32 v30, v33
	v_mov_b32_e32 v29, v33
	v_mov_b32_e32 v28, v33
	v_mov_b32_e32 v27, v33
	v_mov_b32_e32 v26, v33
	v_mov_b32_e32 v65, v33
	v_mov_b32_e32 v64, v33
	v_mov_b32_e32 v63, v33
	v_mov_b32_e32 v62, v33
	v_mov_b32_e32 v61, v33
	v_mov_b32_e32 v60, v33
	v_mov_b32_e32 v59, v33
	v_mov_b32_e32 v58, v33
	v_mov_b32_e32 v9, v33
	v_mov_b32_e32 v8, v33
	v_mov_b32_e32 v7, v33
	v_mov_b32_e32 v6, v33
	v_mov_b32_e32 v5, v33
	v_mov_b32_e32 v4, v33
	v_mov_b32_e32 v3, v33
	v_mov_b32_e32 v2, v33
	v_mov_b32_e32 v73, v33
	v_mov_b32_e32 v72, v33
	v_mov_b32_e32 v71, v33
	v_mov_b32_e32 v70, v33
	v_mov_b32_e32 v69, v33
	v_mov_b32_e32 v68, v33
	v_mov_b32_e32 v67, v33
	v_mov_b32_e32 v66, v33
	v_mov_b32_e32 v17, v33
	v_mov_b32_e32 v16, v33
	v_mov_b32_e32 v15, v33
	v_mov_b32_e32 v14, v33
	v_mov_b32_e32 v13, v33
	v_mov_b32_e32 v12, v33
	v_mov_b32_e32 v11, v33
	v_mov_b32_e32 v10, v33
	v_mov_b32_e32 v81, v33
	v_mov_b32_e32 v80, v33
	v_mov_b32_e32 v79, v33
	v_mov_b32_e32 v78, v33
	v_mov_b32_e32 v77, v33
	v_mov_b32_e32 v76, v33
	v_mov_b32_e32 v75, v33
	v_mov_b32_e32 v74, v33
	v_mov_b32_e32 v25, v33
	v_mov_b32_e32 v24, v33
	v_mov_b32_e32 v23, v33
	v_mov_b32_e32 v22, v33
	v_mov_b32_e32 v21, v33
	v_mov_b32_e32 v20, v33
	v_mov_b32_e32 v19, v33
	v_mov_b32_e32 v18, v33
	v_mov_b32_e32 v89, v33
	v_mov_b32_e32 v88, v33
	v_mov_b32_e32 v87, v33
	v_mov_b32_e32 v86, v33
	v_mov_b32_e32 v85, v33
	v_mov_b32_e32 v84, v33
	v_mov_b32_e32 v83, v33
	v_mov_b32_e32 v82, v33
	v_mov_b32_e32 v41, v33
	v_mov_b32_e32 v40, v33
	v_mov_b32_e32 v39, v33
	v_mov_b32_e32 v38, v33
	v_mov_b32_e32 v37, v33
	v_mov_b32_e32 v36, v33
	v_mov_b32_e32 v35, v33
	v_mov_b32_e32 v34, v33
	v_mov_b32_e32 v97, v33
	v_mov_b32_e32 v96, v33
	v_mov_b32_e32 v95, v33
	v_mov_b32_e32 v94, v33
	v_mov_b32_e32 v93, v33
	v_mov_b32_e32 v92, v33
	v_mov_b32_e32 v91, v33
	v_mov_b32_e32 v90, v33
	v_mov_b32_e32 v49, v33
	v_mov_b32_e32 v48, v33
	v_mov_b32_e32 v47, v33
	v_mov_b32_e32 v46, v33
	v_mov_b32_e32 v45, v33
	v_mov_b32_e32 v44, v33
	v_mov_b32_e32 v43, v33
	v_mov_b32_e32 v42, v33
	v_mov_b32_e32 v105, v33
	v_mov_b32_e32 v104, v33
	v_mov_b32_e32 v103, v33
	v_mov_b32_e32 v102, v33
	v_mov_b32_e32 v101, v33
	v_mov_b32_e32 v100, v33
	v_mov_b32_e32 v99, v33
	v_mov_b32_e32 v98, v33
	v_mov_b32_e32 v57, v33
	v_mov_b32_e32 v56, v33
	v_mov_b32_e32 v55, v33
	v_mov_b32_e32 v54, v33
	v_mov_b32_e32 v53, v33
	v_mov_b32_e32 v52, v33
	v_mov_b32_e32 v51, v33
	v_mov_b32_e32 v50, v33
	v_mov_b32_e32 v113, v33
	v_mov_b32_e32 v112, v33
	v_mov_b32_e32 v111, v33
	v_mov_b32_e32 v110, v33
	v_mov_b32_e32 v109, v33
	v_mov_b32_e32 v108, v33
	v_mov_b32_e32 v107, v33
	v_mov_b32_e32 v106, v33
	v_lshrrev_b32_e32 v138, 4, v136
	s_cbranch_vccnz .LBB5_12
	v_mul_u32_u24_e32 v137, 0x70, v135
	s_ashr_i32 s0, s8, 31
	v_or_b32_e32 v2, v137, v1
	v_lshrrev_b32_e32 v3, 1, v0
	v_bfe_u32 v4, v0, 1, 3
	s_lshr_b32 s0, s0, 26
	v_bitop3_b32 v3, v138, v3, 7 bitop3:0x78
	v_lshlrev_b32_e32 v143, 7, v2
	v_bitop3_b32 v2, v138, v4, 4 bitop3:0x36
	v_add_u32_e32 v106, v126, v132
	v_mov_b32_e32 v107, 0
	s_add_i32 s8, s8, s0
	v_lshlrev_b32_e32 v142, 4, v3
	v_lshlrev_b32_e32 v144, 4, v2
	v_lshl_add_u64 v[2:3], v[106:107], 1, s[52:53]
	s_mov_b64 s[0:1], 0x61a800
	v_add_u32_e32 v106, v128, v132
	v_lshlrev_b32_e32 v140, 13, v127
	v_lshl_add_u64 v[126:127], v[2:3], 0, s[0:1]
	v_lshl_add_u64 v[2:3], v[106:107], 1, s[52:53]
	v_add_u32_e32 v106, v130, v132
	v_lshl_add_u64 v[128:129], v[2:3], 0, s[0:1]
	v_lshl_add_u64 v[2:3], v[106:107], 1, s[52:53]
	v_add_u32_e32 v106, v133, v132
	v_lshl_add_u64 v[130:131], v[2:3], 0, s[0:1]
	v_lshl_add_u64 v[2:3], v[106:107], 1, s[52:53]
	s_mov_b32 s7, 0
	s_ashr_i32 s11, s8, 6
	v_lshlrev_b32_e32 v141, 7, v1
	v_lshl_add_u64 v[132:133], v[2:3], 0, s[0:1]
	s_mov_b32 s6, 64
	s_mov_b32 s12, s7
	v_mov_b32_e32 v106, v107
	v_mov_b32_e32 v108, v107
	v_mov_b32_e32 v109, v107
	v_mov_b32_e32 v110, v107
	v_mov_b32_e32 v111, v107
	v_mov_b32_e32 v112, v107
	v_mov_b32_e32 v113, v107
	v_mov_b32_e32 v50, v107
	v_mov_b32_e32 v51, v107
	v_mov_b32_e32 v52, v107
	v_mov_b32_e32 v53, v107
	v_mov_b32_e32 v54, v107
	v_mov_b32_e32 v55, v107
	v_mov_b32_e32 v56, v107
	v_mov_b32_e32 v57, v107
	v_mov_b32_e32 v98, v107
	v_mov_b32_e32 v99, v107
	v_mov_b32_e32 v100, v107
	v_mov_b32_e32 v101, v107
	v_mov_b32_e32 v102, v107
	v_mov_b32_e32 v103, v107
	v_mov_b32_e32 v104, v107
	v_mov_b32_e32 v105, v107
	v_mov_b32_e32 v42, v107
	v_mov_b32_e32 v43, v107
	v_mov_b32_e32 v44, v107
	v_mov_b32_e32 v45, v107
	v_mov_b32_e32 v46, v107
	v_mov_b32_e32 v47, v107
	v_mov_b32_e32 v48, v107
	v_mov_b32_e32 v49, v107
	v_mov_b32_e32 v90, v107
	v_mov_b32_e32 v91, v107
	v_mov_b32_e32 v92, v107
	v_mov_b32_e32 v93, v107
	v_mov_b32_e32 v94, v107
	v_mov_b32_e32 v95, v107
	v_mov_b32_e32 v96, v107
	v_mov_b32_e32 v97, v107
	v_mov_b32_e32 v34, v107
	v_mov_b32_e32 v35, v107
	v_mov_b32_e32 v36, v107
	v_mov_b32_e32 v37, v107
	v_mov_b32_e32 v38, v107
	v_mov_b32_e32 v39, v107
	v_mov_b32_e32 v40, v107
	v_mov_b32_e32 v41, v107
	v_mov_b32_e32 v82, v107
	v_mov_b32_e32 v83, v107
	v_mov_b32_e32 v84, v107
	v_mov_b32_e32 v85, v107
	v_mov_b32_e32 v86, v107
	v_mov_b32_e32 v87, v107
	v_mov_b32_e32 v88, v107
	v_mov_b32_e32 v89, v107
	v_mov_b32_e32 v18, v107
	v_mov_b32_e32 v19, v107
	v_mov_b32_e32 v20, v107
	v_mov_b32_e32 v21, v107
	v_mov_b32_e32 v22, v107
	v_mov_b32_e32 v23, v107
	v_mov_b32_e32 v24, v107
	v_mov_b32_e32 v25, v107
	v_mov_b32_e32 v74, v107
	v_mov_b32_e32 v75, v107
	v_mov_b32_e32 v76, v107
	v_mov_b32_e32 v77, v107
	v_mov_b32_e32 v78, v107
	v_mov_b32_e32 v79, v107
	v_mov_b32_e32 v80, v107
	v_mov_b32_e32 v81, v107
	v_mov_b32_e32 v10, v107
	v_mov_b32_e32 v11, v107
	v_mov_b32_e32 v12, v107
	v_mov_b32_e32 v13, v107
	v_mov_b32_e32 v14, v107
	v_mov_b32_e32 v15, v107
	v_mov_b32_e32 v16, v107
	v_mov_b32_e32 v17, v107
	v_mov_b32_e32 v66, v107
	v_mov_b32_e32 v67, v107
	v_mov_b32_e32 v68, v107
	v_mov_b32_e32 v69, v107
	v_mov_b32_e32 v70, v107
	v_mov_b32_e32 v71, v107
	v_mov_b32_e32 v72, v107
	v_mov_b32_e32 v73, v107
	v_mov_b32_e32 v2, v107
	v_mov_b32_e32 v3, v107
	v_mov_b32_e32 v4, v107
	v_mov_b32_e32 v5, v107
	v_mov_b32_e32 v6, v107
	v_mov_b32_e32 v7, v107
	v_mov_b32_e32 v8, v107
	v_mov_b32_e32 v9, v107
	v_mov_b32_e32 v58, v107
	v_mov_b32_e32 v59, v107
	v_mov_b32_e32 v60, v107
	v_mov_b32_e32 v61, v107
	v_mov_b32_e32 v62, v107
	v_mov_b32_e32 v63, v107
	v_mov_b32_e32 v64, v107
	v_mov_b32_e32 v65, v107
	v_mov_b32_e32 v26, v107
	v_mov_b32_e32 v27, v107
	v_mov_b32_e32 v28, v107
	v_mov_b32_e32 v29, v107
	v_mov_b32_e32 v30, v107
	v_mov_b32_e32 v31, v107
	v_mov_b32_e32 v32, v107
	v_mov_b32_e32 v33, v107
	v_readfirstlane_b32 s75, v139
	s_cmp_lg_u64 s[4:5], 0
	s_cselect_b32 s92, 1, 0
	s_mov_b32 s72, 0x80
	s_mov_b32 s73, 0
	s_add_u32 s8, s54, 0x80
	s_addc_u32 s9, s55, 0
	s_add_i32 s76, s75, 0x0
	s_add_i32 s77, s75, 0x2000
	s_add_i32 s78, s75, 0x4000
	s_add_i32 s79, s75, 0x6000
	s_add_i32 s80, s75, 0x7000
	s_add_i32 s81, s75, 0x9000
	s_add_i32 s82, s75, 0xb000
	s_add_i32 s83, s75, 0xd000
	s_add_i32 s84, s75, 0xf000
	s_add_i32 s85, s75, 0x11000
	s_add_i32 s86, s75, 0x13000
	s_add_i32 s87, s75, 0x15000
	s_add_i32 s88, s75, 0x16000
	s_add_i32 s89, s75, 0x18000
	s_add_i32 s90, s75, 0x1a000
	s_add_i32 s91, s75, 0x1c000
	v_lshl_add_u64 v[118:119], v[118:119], 1, s[8:9]
	v_lshl_add_u64 v[120:121], v[120:121], 1, s[8:9]
	v_lshl_add_u64 v[122:123], v[122:123], 1, s[8:9]
	v_lshl_add_u64 v[124:125], v[124:125], 1, s[8:9]
	v_add_u32_e32 v234, v142, v143
	v_add_u32_e32 v235, v144, v143
	v_add_u32_e32 v145, v140, v141
	v_add_u32_e32 v236, v142, v145
	v_add_u32_e32 v237, v144, v145
	v_add_u32_e32 v140, 0xf000, v234
	v_add_u32_e32 v141, 0xf000, v235
	v_add_u32_e32 v142, 0xf000, v236
	v_add_u32_e32 v143, 0xf000, v237
	s_lshr_b32 s93, s11, 1
	s_sub_i32 s93, s93, 1
	s_waitcnt vmcnt(0)
	s_barrier
	s_mov_b32 m0, s84
	s_nop 0
	global_load_lds_dwordx4 v[126:127], off nt
	v_lshl_add_u64 v[126:127], v[126:127], 0, s[0:1]
	s_mov_b32 m0, s85
	s_nop 0
	global_load_lds_dwordx4 v[128:129], off nt
	v_lshl_add_u64 v[128:129], v[128:129], 0, s[0:1]
	s_mov_b32 m0, s86
	s_nop 0
	global_load_lds_dwordx4 v[130:131], off nt
	v_lshl_add_u64 v[130:131], v[130:131], 0, s[0:1]
	s_mov_b32 m0, s87
	s_nop 0
	s_cmp_eq_u32 s92, 0
	s_cbranch_scc1 .Lgp_skip_1
	global_load_lds_dwordx4 v[132:133], off nt
.Lgp_skip_1:
	v_lshl_add_u64 v[132:133], v[132:133], 0, s[0:1]
	s_mov_b32 m0, s88
	s_nop 0
	global_load_lds_dwordx4 v[118:119], off
	v_lshl_add_u64 v[118:119], v[118:119], 0, s[72:73]
	s_mov_b32 m0, s89
	s_nop 0
	global_load_lds_dwordx4 v[120:121], off
	v_lshl_add_u64 v[120:121], v[120:121], 0, s[72:73]
	s_mov_b32 m0, s90
	s_nop 0
	global_load_lds_dwordx4 v[122:123], off
	v_lshl_add_u64 v[122:123], v[122:123], 0, s[72:73]
	s_mov_b32 m0, s91
	s_nop 0
	global_load_lds_dwordx4 v[124:125], off
	v_lshl_add_u64 v[124:125], v[124:125], 0, s[72:73]
	ds_read_b128 v[178:181], v236 offset:28672
	ds_read_b128 v[186:189], v236 offset:30720
	ds_read_b128 v[174:177], v236 offset:32768
	ds_read_b128 v[182:185], v236 offset:34816
	ds_read_b128 v[146:149], v234
	ds_read_b128 v[150:153], v234 offset:2048
	ds_read_b128 v[154:157], v234 offset:4096
	ds_read_b128 v[158:161], v234 offset:6144
	ds_read_b128 v[162:165], v234 offset:8192
	ds_read_b128 v[166:169], v234 offset:10240
	ds_read_b128 v[170:173], v234 offset:12288
	ds_read_b128 v[218:221], v237 offset:28672
	ds_read_b128 v[222:225], v237 offset:30720
	ds_read_b128 v[226:229], v237 offset:32768
	ds_read_b128 v[230:233], v237 offset:34816
	ds_read_b128 v[190:193], v235
	ds_read_b128 v[194:197], v235 offset:2048
	ds_read_b128 v[198:201], v235 offset:4096
	ds_read_b128 v[202:205], v235 offset:6144
	ds_read_b128 v[206:209], v235 offset:8192
	ds_read_b128 v[210:213], v235 offset:10240
	ds_read_b128 v[214:217], v235 offset:12288
	s_waitcnt lgkmcnt(11)
	v_mfma_f32_16x16x32_f16 v[110:113], v[146:149], v[178:181], v[110:113]
	v_mfma_f32_16x16x32_f16 v[106:109], v[146:149], v[186:189], v[106:109]
	v_mfma_f32_16x16x32_f16 v[50:53], v[146:149], v[174:177], v[50:53]
	v_mfma_f32_16x16x32_f16 v[54:57], v[146:149], v[182:185], v[54:57]
	v_mfma_f32_16x16x32_f16 v[98:101], v[150:153], v[178:181], v[98:101]
	v_mfma_f32_16x16x32_f16 v[102:105], v[150:153], v[186:189], v[102:105]
	v_mfma_f32_16x16x32_f16 v[42:45], v[150:153], v[174:177], v[42:45]
	v_mfma_f32_16x16x32_f16 v[46:49], v[150:153], v[182:185], v[46:49]
	v_mfma_f32_16x16x32_f16 v[90:93], v[154:157], v[178:181], v[90:93]
	v_mfma_f32_16x16x32_f16 v[94:97], v[154:157], v[186:189], v[94:97]
	v_mfma_f32_16x16x32_f16 v[34:37], v[154:157], v[174:177], v[34:37]
	v_mfma_f32_16x16x32_f16 v[38:41], v[154:157], v[182:185], v[38:41]
	v_mfma_f32_16x16x32_f16 v[82:85], v[158:161], v[178:181], v[82:85]
	v_mfma_f32_16x16x32_f16 v[86:89], v[158:161], v[186:189], v[86:89]
	v_mfma_f32_16x16x32_f16 v[18:21], v[158:161], v[174:177], v[18:21]
	v_mfma_f32_16x16x32_f16 v[22:25], v[158:161], v[182:185], v[22:25]
	v_mfma_f32_16x16x32_f16 v[74:77], v[162:165], v[178:181], v[74:77]
	v_mfma_f32_16x16x32_f16 v[78:81], v[162:165], v[186:189], v[78:81]
	v_mfma_f32_16x16x32_f16 v[10:13], v[162:165], v[174:177], v[10:13]
	v_mfma_f32_16x16x32_f16 v[14:17], v[162:165], v[182:185], v[14:17]
	v_mfma_f32_16x16x32_f16 v[66:69], v[166:169], v[178:181], v[66:69]
	v_mfma_f32_16x16x32_f16 v[70:73], v[166:169], v[186:189], v[70:73]
	v_mfma_f32_16x16x32_f16 v[2:5], v[166:169], v[174:177], v[2:5]
	v_mfma_f32_16x16x32_f16 v[6:9], v[166:169], v[182:185], v[6:9]
	v_mfma_f32_16x16x32_f16 v[58:61], v[170:173], v[178:181], v[58:61]
	v_mfma_f32_16x16x32_f16 v[62:65], v[170:173], v[186:189], v[62:65]
	v_mfma_f32_16x16x32_f16 v[26:29], v[170:173], v[174:177], v[26:29]
	v_mfma_f32_16x16x32_f16 v[30:33], v[170:173], v[182:185], v[30:33]
	s_waitcnt lgkmcnt(0)
	s_waitcnt vmcnt(0)
	s_barrier
.Lgp_loop:
	v_mfma_f32_16x16x32_f16 v[110:113], v[190:193], v[218:221], v[110:113]
	ds_read_b128 v[178:181], v142 offset:28672
	v_mfma_f32_16x16x32_f16 v[106:109], v[190:193], v[222:225], v[106:109]
	ds_read_b128 v[186:189], v142 offset:30720
	v_mfma_f32_16x16x32_f16 v[50:53], v[190:193], v[226:229], v[50:53]
	ds_read_b128 v[174:177], v142 offset:32768
	v_mfma_f32_16x16x32_f16 v[54:57], v[190:193], v[230:233], v[54:57]
	ds_read_b128 v[182:185], v142 offset:34816
	v_mfma_f32_16x16x32_f16 v[98:101], v[194:197], v[218:221], v[98:101]
	ds_read_b128 v[146:149], v140
	v_mfma_f32_16x16x32_f16 v[102:105], v[194:197], v[222:225], v[102:105]
	ds_read_b128 v[150:153], v140 offset:2048
	v_mfma_f32_16x16x32_f16 v[42:45], v[194:197], v[226:229], v[42:45]
	ds_read_b128 v[154:157], v140 offset:4096
	v_mfma_f32_16x16x32_f16 v[46:49], v[194:197], v[230:233], v[46:49]
	ds_read_b128 v[158:161], v140 offset:6144
	v_mfma_f32_16x16x32_f16 v[90:93], v[198:201], v[218:221], v[90:93]
	ds_read_b128 v[162:165], v140 offset:8192
	v_mfma_f32_16x16x32_f16 v[94:97], v[198:201], v[222:225], v[94:97]
	ds_read_b128 v[166:169], v140 offset:10240
	v_mfma_f32_16x16x32_f16 v[34:37], v[198:201], v[226:229], v[34:37]
	ds_read_b128 v[170:173], v140 offset:12288
	v_mfma_f32_16x16x32_f16 v[38:41], v[198:201], v[230:233], v[38:41]
	s_mov_b32 m0, s76
	v_mfma_f32_16x16x32_f16 v[82:85], v[202:205], v[218:221], v[82:85]
	global_load_lds_dwordx4 v[126:127], off nt
	v_lshl_add_u64 v[126:127], v[126:127], 0, s[0:1]
	v_mfma_f32_16x16x32_f16 v[86:89], v[202:205], v[222:225], v[86:89]
	s_mov_b32 m0, s77
	v_mfma_f32_16x16x32_f16 v[18:21], v[202:205], v[226:229], v[18:21]
	global_load_lds_dwordx4 v[128:129], off nt
	v_lshl_add_u64 v[128:129], v[128:129], 0, s[0:1]
	v_mfma_f32_16x16x32_f16 v[22:25], v[202:205], v[230:233], v[22:25]
	s_mov_b32 m0, s78
	v_mfma_f32_16x16x32_f16 v[74:77], v[206:209], v[218:221], v[74:77]
	global_load_lds_dwordx4 v[130:131], off nt
	v_lshl_add_u64 v[130:131], v[130:131], 0, s[0:1]
	v_mfma_f32_16x16x32_f16 v[78:81], v[206:209], v[222:225], v[78:81]
	s_mov_b32 m0, s79
	v_mfma_f32_16x16x32_f16 v[10:13], v[206:209], v[226:229], v[10:13]
	s_cmp_eq_u32 s92, 0
	s_cbranch_scc1 .Lgp_skip_2
	global_load_lds_dwordx4 v[132:133], off nt
.Lgp_skip_2:
	v_lshl_add_u64 v[132:133], v[132:133], 0, s[0:1]
	v_mfma_f32_16x16x32_f16 v[14:17], v[206:209], v[230:233], v[14:17]
	s_mov_b32 m0, s80
	v_mfma_f32_16x16x32_f16 v[66:69], v[210:213], v[218:221], v[66:69]
	global_load_lds_dwordx4 v[118:119], off
	v_lshl_add_u64 v[118:119], v[118:119], 0, s[72:73]
	v_mfma_f32_16x16x32_f16 v[70:73], v[210:213], v[222:225], v[70:73]
	s_mov_b32 m0, s81
	v_mfma_f32_16x16x32_f16 v[2:5], v[210:213], v[226:229], v[2:5]
	global_load_lds_dwordx4 v[120:121], off
	v_lshl_add_u64 v[120:121], v[120:121], 0, s[72:73]
	v_mfma_f32_16x16x32_f16 v[6:9], v[210:213], v[230:233], v[6:9]
	s_mov_b32 m0, s82
	v_mfma_f32_16x16x32_f16 v[58:61], v[214:217], v[218:221], v[58:61]
	global_load_lds_dwordx4 v[122:123], off
	v_lshl_add_u64 v[122:123], v[122:123], 0, s[72:73]
	v_mfma_f32_16x16x32_f16 v[62:65], v[214:217], v[222:225], v[62:65]
	s_mov_b32 m0, s83
	v_mfma_f32_16x16x32_f16 v[26:29], v[214:217], v[226:229], v[26:29]
	global_load_lds_dwordx4 v[124:125], off
	v_lshl_add_u64 v[124:125], v[124:125], 0, s[72:73]
	v_mfma_f32_16x16x32_f16 v[30:33], v[214:217], v[230:233], v[30:33]
	s_waitcnt lgkmcnt(0)
	v_mfma_f32_16x16x32_f16 v[110:113], v[146:149], v[178:181], v[110:113]
	ds_read_b128 v[218:221], v143 offset:28672
	v_mfma_f32_16x16x32_f16 v[106:109], v[146:149], v[186:189], v[106:109]
	ds_read_b128 v[222:225], v143 offset:30720
	v_mfma_f32_16x16x32_f16 v[50:53], v[146:149], v[174:177], v[50:53]
	ds_read_b128 v[226:229], v143 offset:32768
	v_mfma_f32_16x16x32_f16 v[54:57], v[146:149], v[182:185], v[54:57]
	ds_read_b128 v[230:233], v143 offset:34816
	v_mfma_f32_16x16x32_f16 v[98:101], v[150:153], v[178:181], v[98:101]
	ds_read_b128 v[190:193], v141
	v_mfma_f32_16x16x32_f16 v[102:105], v[150:153], v[186:189], v[102:105]
	ds_read_b128 v[194:197], v141 offset:2048
	v_mfma_f32_16x16x32_f16 v[42:45], v[150:153], v[174:177], v[42:45]
	ds_read_b128 v[198:201], v141 offset:4096
	v_mfma_f32_16x16x32_f16 v[46:49], v[150:153], v[182:185], v[46:49]
	ds_read_b128 v[202:205], v141 offset:6144
	v_mfma_f32_16x16x32_f16 v[90:93], v[154:157], v[178:181], v[90:93]
	ds_read_b128 v[206:209], v141 offset:8192
	v_mfma_f32_16x16x32_f16 v[94:97], v[154:157], v[186:189], v[94:97]
	ds_read_b128 v[210:213], v141 offset:10240
	v_mfma_f32_16x16x32_f16 v[34:37], v[154:157], v[174:177], v[34:37]
	ds_read_b128 v[214:217], v141 offset:12288
	v_mfma_f32_16x16x32_f16 v[38:41], v[154:157], v[182:185], v[38:41]
	v_mfma_f32_16x16x32_f16 v[82:85], v[158:161], v[178:181], v[82:85]
	v_mfma_f32_16x16x32_f16 v[86:89], v[158:161], v[186:189], v[86:89]
	v_mfma_f32_16x16x32_f16 v[18:21], v[158:161], v[174:177], v[18:21]
	v_mfma_f32_16x16x32_f16 v[22:25], v[158:161], v[182:185], v[22:25]
	v_mfma_f32_16x16x32_f16 v[74:77], v[162:165], v[178:181], v[74:77]
	v_mfma_f32_16x16x32_f16 v[78:81], v[162:165], v[186:189], v[78:81]
	v_mfma_f32_16x16x32_f16 v[10:13], v[162:165], v[174:177], v[10:13]
	v_mfma_f32_16x16x32_f16 v[14:17], v[162:165], v[182:185], v[14:17]
	v_mfma_f32_16x16x32_f16 v[66:69], v[166:169], v[178:181], v[66:69]
	v_mfma_f32_16x16x32_f16 v[70:73], v[166:169], v[186:189], v[70:73]
	v_mfma_f32_16x16x32_f16 v[2:5], v[166:169], v[174:177], v[2:5]
	v_mfma_f32_16x16x32_f16 v[6:9], v[166:169], v[182:185], v[6:9]
	v_mfma_f32_16x16x32_f16 v[58:61], v[170:173], v[178:181], v[58:61]
	v_mfma_f32_16x16x32_f16 v[62:65], v[170:173], v[186:189], v[62:65]
	v_mfma_f32_16x16x32_f16 v[26:29], v[170:173], v[174:177], v[26:29]
	v_mfma_f32_16x16x32_f16 v[30:33], v[170:173], v[182:185], v[30:33]
	s_waitcnt lgkmcnt(0)
	s_waitcnt vmcnt(0)
	s_barrier
	v_mfma_f32_16x16x32_f16 v[110:113], v[190:193], v[218:221], v[110:113]
	ds_read_b128 v[178:181], v236 offset:28672
	v_mfma_f32_16x16x32_f16 v[106:109], v[190:193], v[222:225], v[106:109]
	ds_read_b128 v[186:189], v236 offset:30720
	v_mfma_f32_16x16x32_f16 v[50:53], v[190:193], v[226:229], v[50:53]
	ds_read_b128 v[174:177], v236 offset:32768
	v_mfma_f32_16x16x32_f16 v[54:57], v[190:193], v[230:233], v[54:57]
	ds_read_b128 v[182:185], v236 offset:34816
	v_mfma_f32_16x16x32_f16 v[98:101], v[194:197], v[218:221], v[98:101]
	ds_read_b128 v[146:149], v234
	v_mfma_f32_16x16x32_f16 v[102:105], v[194:197], v[222:225], v[102:105]
	ds_read_b128 v[150:153], v234 offset:2048
	v_mfma_f32_16x16x32_f16 v[42:45], v[194:197], v[226:229], v[42:45]
	ds_read_b128 v[154:157], v234 offset:4096
	v_mfma_f32_16x16x32_f16 v[46:49], v[194:197], v[230:233], v[46:49]
	ds_read_b128 v[158:161], v234 offset:6144
	v_mfma_f32_16x16x32_f16 v[90:93], v[198:201], v[218:221], v[90:93]
	ds_read_b128 v[162:165], v234 offset:8192
	v_mfma_f32_16x16x32_f16 v[94:97], v[198:201], v[222:225], v[94:97]
	ds_read_b128 v[166:169], v234 offset:10240
	v_mfma_f32_16x16x32_f16 v[34:37], v[198:201], v[226:229], v[34:37]
	ds_read_b128 v[170:173], v234 offset:12288
	v_mfma_f32_16x16x32_f16 v[38:41], v[198:201], v[230:233], v[38:41]
	s_mov_b32 m0, s84
	v_mfma_f32_16x16x32_f16 v[82:85], v[202:205], v[218:221], v[82:85]
	global_load_lds_dwordx4 v[126:127], off nt
	v_lshl_add_u64 v[126:127], v[126:127], 0, s[0:1]
	v_mfma_f32_16x16x32_f16 v[86:89], v[202:205], v[222:225], v[86:89]
	s_mov_b32 m0, s85
	v_mfma_f32_16x16x32_f16 v[18:21], v[202:205], v[226:229], v[18:21]
	global_load_lds_dwordx4 v[128:129], off nt
	v_lshl_add_u64 v[128:129], v[128:129], 0, s[0:1]
	v_mfma_f32_16x16x32_f16 v[22:25], v[202:205], v[230:233], v[22:25]
	s_mov_b32 m0, s86
	v_mfma_f32_16x16x32_f16 v[74:77], v[206:209], v[218:221], v[74:77]
	global_load_lds_dwordx4 v[130:131], off nt
	v_lshl_add_u64 v[130:131], v[130:131], 0, s[0:1]
	v_mfma_f32_16x16x32_f16 v[78:81], v[206:209], v[222:225], v[78:81]
	s_mov_b32 m0, s87
	v_mfma_f32_16x16x32_f16 v[10:13], v[206:209], v[226:229], v[10:13]
	s_cmp_eq_u32 s92, 0
	s_cbranch_scc1 .Lgp_skip_3
	global_load_lds_dwordx4 v[132:133], off nt
.Lgp_skip_3:
	v_lshl_add_u64 v[132:133], v[132:133], 0, s[0:1]
	v_mfma_f32_16x16x32_f16 v[14:17], v[206:209], v[230:233], v[14:17]
	s_mov_b32 m0, s88
	v_mfma_f32_16x16x32_f16 v[66:69], v[210:213], v[218:221], v[66:69]
	global_load_lds_dwordx4 v[118:119], off
	v_lshl_add_u64 v[118:119], v[118:119], 0, s[72:73]
	v_mfma_f32_16x16x32_f16 v[70:73], v[210:213], v[222:225], v[70:73]
	s_mov_b32 m0, s89
	v_mfma_f32_16x16x32_f16 v[2:5], v[210:213], v[226:229], v[2:5]
	global_load_lds_dwordx4 v[120:121], off
	v_lshl_add_u64 v[120:121], v[120:121], 0, s[72:73]
	v_mfma_f32_16x16x32_f16 v[6:9], v[210:213], v[230:233], v[6:9]
	s_mov_b32 m0, s90
	v_mfma_f32_16x16x32_f16 v[58:61], v[214:217], v[218:221], v[58:61]
	global_load_lds_dwordx4 v[122:123], off
	v_lshl_add_u64 v[122:123], v[122:123], 0, s[72:73]
	v_mfma_f32_16x16x32_f16 v[62:65], v[214:217], v[222:225], v[62:65]
	s_mov_b32 m0, s91
	v_mfma_f32_16x16x32_f16 v[26:29], v[214:217], v[226:229], v[26:29]
	global_load_lds_dwordx4 v[124:125], off
	v_lshl_add_u64 v[124:125], v[124:125], 0, s[72:73]
	v_mfma_f32_16x16x32_f16 v[30:33], v[214:217], v[230:233], v[30:33]
	s_waitcnt lgkmcnt(0)
	v_mfma_f32_16x16x32_f16 v[110:113], v[146:149], v[178:181], v[110:113]
	ds_read_b128 v[218:221], v237 offset:28672
	v_mfma_f32_16x16x32_f16 v[106:109], v[146:149], v[186:189], v[106:109]
	ds_read_b128 v[222:225], v237 offset:30720
	v_mfma_f32_16x16x32_f16 v[50:53], v[146:149], v[174:177], v[50:53]
	ds_read_b128 v[226:229], v237 offset:32768
	v_mfma_f32_16x16x32_f16 v[54:57], v[146:149], v[182:185], v[54:57]
	ds_read_b128 v[230:233], v237 offset:34816
	v_mfma_f32_16x16x32_f16 v[98:101], v[150:153], v[178:181], v[98:101]
	ds_read_b128 v[190:193], v235
	v_mfma_f32_16x16x32_f16 v[102:105], v[150:153], v[186:189], v[102:105]
	ds_read_b128 v[194:197], v235 offset:2048
	v_mfma_f32_16x16x32_f16 v[42:45], v[150:153], v[174:177], v[42:45]
	ds_read_b128 v[198:201], v235 offset:4096
	v_mfma_f32_16x16x32_f16 v[46:49], v[150:153], v[182:185], v[46:49]
	ds_read_b128 v[202:205], v235 offset:6144
	v_mfma_f32_16x16x32_f16 v[90:93], v[154:157], v[178:181], v[90:93]
	ds_read_b128 v[206:209], v235 offset:8192
	v_mfma_f32_16x16x32_f16 v[94:97], v[154:157], v[186:189], v[94:97]
	ds_read_b128 v[210:213], v235 offset:10240
	v_mfma_f32_16x16x32_f16 v[34:37], v[154:157], v[174:177], v[34:37]
	ds_read_b128 v[214:217], v235 offset:12288
	v_mfma_f32_16x16x32_f16 v[38:41], v[154:157], v[182:185], v[38:41]
	v_mfma_f32_16x16x32_f16 v[82:85], v[158:161], v[178:181], v[82:85]
	v_mfma_f32_16x16x32_f16 v[86:89], v[158:161], v[186:189], v[86:89]
	v_mfma_f32_16x16x32_f16 v[18:21], v[158:161], v[174:177], v[18:21]
	v_mfma_f32_16x16x32_f16 v[22:25], v[158:161], v[182:185], v[22:25]
	v_mfma_f32_16x16x32_f16 v[74:77], v[162:165], v[178:181], v[74:77]
	v_mfma_f32_16x16x32_f16 v[78:81], v[162:165], v[186:189], v[78:81]
	v_mfma_f32_16x16x32_f16 v[10:13], v[162:165], v[174:177], v[10:13]
	v_mfma_f32_16x16x32_f16 v[14:17], v[162:165], v[182:185], v[14:17]
	v_mfma_f32_16x16x32_f16 v[66:69], v[166:169], v[178:181], v[66:69]
	v_mfma_f32_16x16x32_f16 v[70:73], v[166:169], v[186:189], v[70:73]
	v_mfma_f32_16x16x32_f16 v[2:5], v[166:169], v[174:177], v[2:5]
	v_mfma_f32_16x16x32_f16 v[6:9], v[166:169], v[182:185], v[6:9]
	v_mfma_f32_16x16x32_f16 v[58:61], v[170:173], v[178:181], v[58:61]
	v_mfma_f32_16x16x32_f16 v[62:65], v[170:173], v[186:189], v[62:65]
	v_mfma_f32_16x16x32_f16 v[26:29], v[170:173], v[174:177], v[26:29]
	v_mfma_f32_16x16x32_f16 v[30:33], v[170:173], v[182:185], v[30:33]
	s_waitcnt lgkmcnt(0)
	s_waitcnt vmcnt(0)
	s_barrier
	s_sub_i32 s93, s93, 1
	s_cmp_lg_u32 s93, 0
	s_cbranch_scc1 .Lgp_loop
	v_mfma_f32_16x16x32_f16 v[110:113], v[190:193], v[218:221], v[110:113]
	ds_read_b128 v[178:181], v142 offset:28672
	v_mfma_f32_16x16x32_f16 v[106:109], v[190:193], v[222:225], v[106:109]
	ds_read_b128 v[186:189], v142 offset:30720
	v_mfma_f32_16x16x32_f16 v[50:53], v[190:193], v[226:229], v[50:53]
	ds_read_b128 v[174:177], v142 offset:32768
	v_mfma_f32_16x16x32_f16 v[54:57], v[190:193], v[230:233], v[54:57]
	ds_read_b128 v[182:185], v142 offset:34816
	v_mfma_f32_16x16x32_f16 v[98:101], v[194:197], v[218:221], v[98:101]
	ds_read_b128 v[146:149], v140
	v_mfma_f32_16x16x32_f16 v[102:105], v[194:197], v[222:225], v[102:105]
	ds_read_b128 v[150:153], v140 offset:2048
	v_mfma_f32_16x16x32_f16 v[42:45], v[194:197], v[226:229], v[42:45]
	ds_read_b128 v[154:157], v140 offset:4096
	v_mfma_f32_16x16x32_f16 v[46:49], v[194:197], v[230:233], v[46:49]
	ds_read_b128 v[158:161], v140 offset:6144
	v_mfma_f32_16x16x32_f16 v[90:93], v[198:201], v[218:221], v[90:93]
	ds_read_b128 v[162:165], v140 offset:8192
	v_mfma_f32_16x16x32_f16 v[94:97], v[198:201], v[222:225], v[94:97]
	ds_read_b128 v[166:169], v140 offset:10240
	v_mfma_f32_16x16x32_f16 v[34:37], v[198:201], v[226:229], v[34:37]
	ds_read_b128 v[170:173], v140 offset:12288
	v_mfma_f32_16x16x32_f16 v[38:41], v[198:201], v[230:233], v[38:41]
	v_mfma_f32_16x16x32_f16 v[82:85], v[202:205], v[218:221], v[82:85]
	v_mfma_f32_16x16x32_f16 v[86:89], v[202:205], v[222:225], v[86:89]
	v_mfma_f32_16x16x32_f16 v[18:21], v[202:205], v[226:229], v[18:21]
	v_mfma_f32_16x16x32_f16 v[22:25], v[202:205], v[230:233], v[22:25]
	v_mfma_f32_16x16x32_f16 v[74:77], v[206:209], v[218:221], v[74:77]
	v_mfma_f32_16x16x32_f16 v[78:81], v[206:209], v[222:225], v[78:81]
	v_mfma_f32_16x16x32_f16 v[10:13], v[206:209], v[226:229], v[10:13]
	v_mfma_f32_16x16x32_f16 v[14:17], v[206:209], v[230:233], v[14:17]
	v_mfma_f32_16x16x32_f16 v[66:69], v[210:213], v[218:221], v[66:69]
	v_mfma_f32_16x16x32_f16 v[70:73], v[210:213], v[222:225], v[70:73]
	v_mfma_f32_16x16x32_f16 v[2:5], v[210:213], v[226:229], v[2:5]
	v_mfma_f32_16x16x32_f16 v[6:9], v[210:213], v[230:233], v[6:9]
	v_mfma_f32_16x16x32_f16 v[58:61], v[214:217], v[218:221], v[58:61]
	v_mfma_f32_16x16x32_f16 v[62:65], v[214:217], v[222:225], v[62:65]
	v_mfma_f32_16x16x32_f16 v[26:29], v[214:217], v[226:229], v[26:29]
	v_mfma_f32_16x16x32_f16 v[30:33], v[214:217], v[230:233], v[30:33]
	s_waitcnt lgkmcnt(0)
	v_mfma_f32_16x16x32_f16 v[110:113], v[146:149], v[178:181], v[110:113]
	ds_read_b128 v[218:221], v143 offset:28672
	v_mfma_f32_16x16x32_f16 v[106:109], v[146:149], v[186:189], v[106:109]
	ds_read_b128 v[222:225], v143 offset:30720
	v_mfma_f32_16x16x32_f16 v[50:53], v[146:149], v[174:177], v[50:53]
	ds_read_b128 v[226:229], v143 offset:32768
	v_mfma_f32_16x16x32_f16 v[54:57], v[146:149], v[182:185], v[54:57]
	ds_read_b128 v[230:233], v143 offset:34816
	v_mfma_f32_16x16x32_f16 v[98:101], v[150:153], v[178:181], v[98:101]
	ds_read_b128 v[190:193], v141
	v_mfma_f32_16x16x32_f16 v[102:105], v[150:153], v[186:189], v[102:105]
	ds_read_b128 v[194:197], v141 offset:2048
	v_mfma_f32_16x16x32_f16 v[42:45], v[150:153], v[174:177], v[42:45]
	ds_read_b128 v[198:201], v141 offset:4096
	v_mfma_f32_16x16x32_f16 v[46:49], v[150:153], v[182:185], v[46:49]
	ds_read_b128 v[202:205], v141 offset:6144
	v_mfma_f32_16x16x32_f16 v[90:93], v[154:157], v[178:181], v[90:93]
	ds_read_b128 v[206:209], v141 offset:8192
	v_mfma_f32_16x16x32_f16 v[94:97], v[154:157], v[186:189], v[94:97]
	ds_read_b128 v[210:213], v141 offset:10240
	v_mfma_f32_16x16x32_f16 v[34:37], v[154:157], v[174:177], v[34:37]
	ds_read_b128 v[214:217], v141 offset:12288
	v_mfma_f32_16x16x32_f16 v[38:41], v[154:157], v[182:185], v[38:41]
	v_mfma_f32_16x16x32_f16 v[82:85], v[158:161], v[178:181], v[82:85]
	v_mfma_f32_16x16x32_f16 v[86:89], v[158:161], v[186:189], v[86:89]
	v_mfma_f32_16x16x32_f16 v[18:21], v[158:161], v[174:177], v[18:21]
	v_mfma_f32_16x16x32_f16 v[22:25], v[158:161], v[182:185], v[22:25]
	v_mfma_f32_16x16x32_f16 v[74:77], v[162:165], v[178:181], v[74:77]
	v_mfma_f32_16x16x32_f16 v[78:81], v[162:165], v[186:189], v[78:81]
	v_mfma_f32_16x16x32_f16 v[10:13], v[162:165], v[174:177], v[10:13]
	v_mfma_f32_16x16x32_f16 v[14:17], v[162:165], v[182:185], v[14:17]
	v_mfma_f32_16x16x32_f16 v[66:69], v[166:169], v[178:181], v[66:69]
	v_mfma_f32_16x16x32_f16 v[70:73], v[166:169], v[186:189], v[70:73]
	v_mfma_f32_16x16x32_f16 v[2:5], v[166:169], v[174:177], v[2:5]
	v_mfma_f32_16x16x32_f16 v[6:9], v[166:169], v[182:185], v[6:9]
	v_mfma_f32_16x16x32_f16 v[58:61], v[170:173], v[178:181], v[58:61]
	v_mfma_f32_16x16x32_f16 v[62:65], v[170:173], v[186:189], v[62:65]
	v_mfma_f32_16x16x32_f16 v[26:29], v[170:173], v[174:177], v[26:29]
	v_mfma_f32_16x16x32_f16 v[30:33], v[170:173], v[182:185], v[30:33]
	s_waitcnt lgkmcnt(0)
	v_mfma_f32_16x16x32_f16 v[110:113], v[190:193], v[218:221], v[110:113]
	v_mfma_f32_16x16x32_f16 v[106:109], v[190:193], v[222:225], v[106:109]
	v_mfma_f32_16x16x32_f16 v[50:53], v[190:193], v[226:229], v[50:53]
	v_mfma_f32_16x16x32_f16 v[54:57], v[190:193], v[230:233], v[54:57]
	v_mfma_f32_16x16x32_f16 v[98:101], v[194:197], v[218:221], v[98:101]
	v_mfma_f32_16x16x32_f16 v[102:105], v[194:197], v[222:225], v[102:105]
	v_mfma_f32_16x16x32_f16 v[42:45], v[194:197], v[226:229], v[42:45]
	v_mfma_f32_16x16x32_f16 v[46:49], v[194:197], v[230:233], v[46:49]
	v_mfma_f32_16x16x32_f16 v[90:93], v[198:201], v[218:221], v[90:93]
	v_mfma_f32_16x16x32_f16 v[94:97], v[198:201], v[222:225], v[94:97]
	v_mfma_f32_16x16x32_f16 v[34:37], v[198:201], v[226:229], v[34:37]
	v_mfma_f32_16x16x32_f16 v[38:41], v[198:201], v[230:233], v[38:41]
	v_mfma_f32_16x16x32_f16 v[82:85], v[202:205], v[218:221], v[82:85]
	v_mfma_f32_16x16x32_f16 v[86:89], v[202:205], v[222:225], v[86:89]
	v_mfma_f32_16x16x32_f16 v[18:21], v[202:205], v[226:229], v[18:21]
	v_mfma_f32_16x16x32_f16 v[22:25], v[202:205], v[230:233], v[22:25]
	v_mfma_f32_16x16x32_f16 v[74:77], v[206:209], v[218:221], v[74:77]
	v_mfma_f32_16x16x32_f16 v[78:81], v[206:209], v[222:225], v[78:81]
	v_mfma_f32_16x16x32_f16 v[10:13], v[206:209], v[226:229], v[10:13]
	v_mfma_f32_16x16x32_f16 v[14:17], v[206:209], v[230:233], v[14:17]
	v_mfma_f32_16x16x32_f16 v[66:69], v[210:213], v[218:221], v[66:69]
	v_mfma_f32_16x16x32_f16 v[70:73], v[210:213], v[222:225], v[70:73]
	v_mfma_f32_16x16x32_f16 v[2:5], v[210:213], v[226:229], v[2:5]
	v_mfma_f32_16x16x32_f16 v[6:9], v[210:213], v[230:233], v[6:9]
	v_mfma_f32_16x16x32_f16 v[58:61], v[214:217], v[218:221], v[58:61]
	v_mfma_f32_16x16x32_f16 v[62:65], v[214:217], v[222:225], v[62:65]
	v_mfma_f32_16x16x32_f16 v[26:29], v[214:217], v[226:229], v[26:29]
	v_mfma_f32_16x16x32_f16 v[30:33], v[214:217], v[230:233], v[30:33]

	.amdhsa_kernel _Z6k_gemm8GemmProbS_
		.amdhsa_group_segment_fixed_size 0
		.amdhsa_private_segment_fixed_size 0
		.amdhsa_kernarg_size 96
		.amdhsa_user_sgpr_count 2
		.amdhsa_user_sgpr_dispatch_ptr 0
		.amdhsa_user_sgpr_queue_ptr 0
		.amdhsa_user_sgpr_kernarg_segment_ptr 1
		.amdhsa_user_sgpr_dispatch_id 0
		.amdhsa_user_sgpr_kernarg_preload_length 0
		.amdhsa_user_sgpr_kernarg_preload_offset 0
		.amdhsa_user_sgpr_private_segment_size 0
		.amdhsa_uses_dynamic_stack 0
		.amdhsa_enable_private_segment 0
		.amdhsa_system_sgpr_workgroup_id_x 1
		.amdhsa_system_sgpr_workgroup_id_y 0
		.amdhsa_system_sgpr_workgroup_id_z 0
		.amdhsa_system_sgpr_workgroup_info 0
		.amdhsa_system_vgpr_workitem_id 0
		.amdhsa_next_free_vgpr 240
		.amdhsa_next_free_sgpr 94
		.amdhsa_accum_offset 240
		.amdhsa_reserve_vcc 1
		.amdhsa_float_round_mode_32 0
		.amdhsa_float_round_mode_16_64 0
		.amdhsa_float_denorm_mode_32 3
		.amdhsa_float_denorm_mode_16_64 3
		.amdhsa_dx10_clamp 1
		.amdhsa_ieee_mode 1
		.amdhsa_fp16_overflow 0
		.amdhsa_tg_split 0
		.amdhsa_exception_fp_ieee_invalid_op 0
		.amdhsa_exception_fp_denorm_src 0
		.amdhsa_exception_fp_ieee_div_zero 0
		.amdhsa_exception_fp_ieee_overflow 0
		.amdhsa_exception_fp_ieee_underflow 0
		.amdhsa_exception_fp_ieee_inexact 0
		.amdhsa_exception_int_div_zero 0
	.end_amdhsa_kernel

.LBB6_17:
	s_endpgm
	.p2alignl 8, 3212836864

	.text
	.p2alignl 6, 3212836864
	.fill 256, 4, 3212836864
	.p2alignl 8, 3212836864

amdhsa.kernels:
  - .agpr_count:     0
    .args:
      - .offset:         0
        .size:           336
        .value_kind:     by_value
    .group_segment_fixed_size: 1024
    .kernarg_segment_align: 8
    .kernarg_segment_size: 336
    .language:       OpenCL C
    .language_version:
      - 2
      - 0
    .max_flat_workgroup_size: 256
    .name:           _Z6k_prep8PrepArgs
    .private_segment_fixed_size: 0
    .sgpr_count:     30
    .sgpr_spill_count: 0
    .symbol:         _Z6k_prep8PrepArgs.kd
    .uniform_work_group_size: 1
    .uses_dynamic_stack: false
    .vgpr_count:     20
    .vgpr_spill_count: 0
    .wavefront_size: 64
  - .agpr_count:     0
    .args:
      - .address_space:  global
        .offset:         0
        .size:           8
        .value_kind:     global_buffer
      - .actual_access:  write_only
        .address_space:  global
        .offset:         8
        .size:           8
        .value_kind:     global_buffer
    .group_segment_fixed_size: 16
    .kernarg_segment_align: 8
    .kernarg_segment_size: 16
    .language:       OpenCL C
    .language_version:
      - 2
      - 0
    .max_flat_workgroup_size: 256
    .name:           _Z7k_bscanPiS_
    .private_segment_fixed_size: 0
    .sgpr_count:     22
    .sgpr_spill_count: 0
    .symbol:         _Z7k_bscanPiS_.kd
    .uniform_work_group_size: 1
    .uses_dynamic_stack: false
    .vgpr_count:     18
    .vgpr_spill_count: 0
    .wavefront_size: 64
  - .agpr_count:     16
    .args:
      - .offset:         0
        .size:           24
        .value_kind:     by_value
      - .actual_access:  read_only
        .address_space:  global
        .offset:         24
        .size:           8
        .value_kind:     global_buffer
      - .actual_access:  read_only
        .address_space:  global
        .offset:         32
        .size:           8
        .value_kind:     global_buffer
      - .actual_access:  write_only
        .address_space:  global
        .offset:         40
        .size:           8
        .value_kind:     global_buffer
      - .offset:         48
        .size:           608
        .value_kind:     by_value
      - .actual_access:  read_only
        .address_space:  global
        .offset:         656
        .size:           8
        .value_kind:     global_buffer
      - .actual_access:  write_only
        .address_space:  global
        .offset:         664
        .size:           8
        .value_kind:     global_buffer
    .group_segment_fixed_size: 33024
    .kernarg_segment_align: 8
    .kernarg_segment_size: 672
    .language:       OpenCL C
    .language_version:
      - 2
      - 0
    .max_flat_workgroup_size: 256
    .name:           _Z9k_scatter8EdgePtrsPKiS1_Pj8FoldArgsPKfPDF16_
    .private_segment_fixed_size: 0
    .sgpr_count:     28
    .sgpr_spill_count: 0
    .symbol:         _Z9k_scatter8EdgePtrsPKiS1_Pj8FoldArgsPKfPDF16_.kd
    .uniform_work_group_size: 1
    .uses_dynamic_stack: false
    .vgpr_count:     116
    .vgpr_spill_count: 0
    .wavefront_size: 64
  - .agpr_count:     0
    .args:
      - .actual_access:  read_only
        .address_space:  global
        .offset:         0
        .size:           8
        .value_kind:     global_buffer
      - .actual_access:  read_only
        .address_space:  global
        .offset:         8
        .size:           8
        .value_kind:     global_buffer
      - .actual_access:  write_only
        .address_space:  global
        .offset:         16
        .size:           8
        .value_kind:     global_buffer
      - .actual_access:  write_only
        .address_space:  global
        .offset:         24
        .size:           8
        .value_kind:     global_buffer
      - .actual_access:  read_only
        .address_space:  global
        .offset:         32
        .size:           8
        .value_kind:     global_buffer
      - .actual_access:  write_only
        .address_space:  global
        .offset:         40
        .size:           8
        .value_kind:     global_buffer
    .group_segment_fixed_size: 1048
    .kernarg_segment_align: 8
    .kernarg_segment_size: 48
    .language:       OpenCL C
    .language_version:
      - 2
      - 0
    .max_flat_workgroup_size: 256
    .name:           _Z6k_finePKiPKjPiPtPKfPDF16_
    .private_segment_fixed_size: 0
    .sgpr_count:     47
    .sgpr_spill_count: 0
    .symbol:         _Z6k_finePKiPKjPiPtPKfPDF16_.kd
    .uniform_work_group_size: 1
    .uses_dynamic_stack: false
    .vgpr_count:     28
    .vgpr_spill_count: 0
    .wavefront_size: 64
  - .agpr_count:     0
    .args:
      - .offset:         0
        .size:           40
        .value_kind:     by_value
      - .offset:         40
        .size:           40
        .value_kind:     by_value
      - .offset:         80
        .size:           40
        .value_kind:     by_value
    .group_segment_fixed_size: 0
    .kernarg_segment_align: 8
    .kernarg_segment_size: 120
    .language:       OpenCL C
    .language_version:
      - 2
      - 0
    .max_flat_workgroup_size: 256
    .name:           _Z5k_agg6AggJobS_S_
    .private_segment_fixed_size: 0
    .sgpr_count:     34
    .sgpr_spill_count: 0
    .symbol:         _Z5k_agg6AggJobS_S_.kd
    .uniform_work_group_size: 1
    .uses_dynamic_stack: false
    .vgpr_count:     60
    .vgpr_spill_count: 0
    .wavefront_size: 64
  - .agpr_count:     0
    .args:
      - .offset:         0
        .size:           48
        .value_kind:     by_value
      - .offset:         48
        .size:           48
        .value_kind:     by_value
    .group_segment_fixed_size: 0
    .kernarg_segment_align: 8
    .kernarg_segment_size: 96
    .language:       OpenCL C
    .language_version:
      - 2
      - 0
    .max_flat_workgroup_size: 512
    .name:           _Z6k_gemm8GemmProbS_
    .private_segment_fixed_size: 0
    .sgpr_count:     100
    .sgpr_spill_count: 0
    .symbol:         _Z6k_gemm8GemmProbS_.kd
    .uniform_work_group_size: 1
    .uses_dynamic_stack: false
    .vgpr_count:     240
    .vgpr_spill_count: 0
    .wavefront_size: 64
  - .agpr_count:     0
    .args:
      - .actual_access:  read_only
        .address_space:  global
        .offset:         0
        .size:           8
        .value_kind:     global_buffer
      - .actual_access:  read_only
        .address_space:  global
        .offset:         8
        .size:           8
        .value_kind:     global_buffer
      - .actual_access:  read_only
        .address_space:  global
        .offset:         16
        .size:           8
        .value_kind:     global_buffer
      - .actual_access:  read_only
        .address_space:  global
        .offset:         24
        .size:           8
        .value_kind:     global_buffer
      - .actual_access:  write_only
        .address_space:  global
        .offset:         32
        .size:           8
        .value_kind:     global_buffer
      - .offset:         40
        .size:           8
        .value_kind:     by_value
    .group_segment_fixed_size: 2048
    .kernarg_segment_align: 8
    .kernarg_segment_size: 48
    .language:       OpenCL C
    .language_version:
      - 2
      - 0
    .max_flat_workgroup_size: 256
    .name:           _Z6k_normILb0EEvPKDF16_PKdPKfS5_Pvm
    .private_segment_fixed_size: 0
    .sgpr_count:     23
    .sgpr_spill_count: 0
    .symbol:         _Z6k_normILb0EEvPKDF16_PKdPKfS5_Pvm.kd
    .uniform_work_group_size: 1
    .uses_dynamic_stack: false
    .vgpr_count:     56
    .vgpr_spill_count: 0
    .wavefront_size: 64
  - .agpr_count:     0
    .args:
      - .actual_access:  read_only
        .address_space:  global
        .offset:         0
        .size:           8
        .value_kind:     global_buffer
      - .actual_access:  read_only
        .address_space:  global
        .offset:         8
        .size:           8
        .value_kind:     global_buffer
      - .actual_access:  read_only
        .address_space:  global
        .offset:         16
        .size:           8
        .value_kind:     global_buffer
      - .actual_access:  read_only
        .address_space:  global
        .offset:         24
        .size:           8
        .value_kind:     global_buffer
      - .actual_access:  write_only
        .address_space:  global
        .offset:         32
        .size:           8
        .value_kind:     global_buffer
      - .offset:         40
        .size:           8
        .value_kind:     by_value
    .group_segment_fixed_size: 2048
    .kernarg_segment_align: 8
    .kernarg_segment_size: 48
    .language:       OpenCL C
    .language_version:
      - 2
      - 0
    .max_flat_workgroup_size: 256
    .name:           _Z6k_normILb1EEvPKDF16_PKdPKfS5_Pvm
    .private_segment_fixed_size: 0
    .sgpr_count:     23
    .sgpr_spill_count: 0
    .symbol:         _Z6k_normILb1EEvPKDF16_PKdPKfS5_Pvm.kd
    .uniform_work_group_size: 1
    .uses_dynamic_stack: false
    .vgpr_count:     52
    .vgpr_spill_count: 0
    .wavefront_size: 64
